# MoE K loops: one static priority raise (s_setprio 1) for waves 4-7 for the whole of P7/P8, reset before P9
# baseline (speedup 1.0000x reference)
; #define LAS __attribute__((address_space(3)))
;     template <class Tp> __device__ __forceinline__ Tp* w(size_t off) const { return (Tp*)(ws + off); }
; __device__ __forceinline__ void ph_moe1(const Frame& F) {
;     LAS int* offs = (LAS int*)(F.lds + LDS_TAB); LAS int* cnts = offs + 128; LAS int* rt_exp = offs + 256;
;     expert_offsets(F, offs, cnts, rt_exp);
;     pg8::GroupedOrder So; So.init(rt_exp, (offs[64] >> 8) * 8, (int)gridDim.x, (int)blockIdx.x);
;     pg8::EpiSwiGLU E{F.w<bf16>(WS_HID)};
;     pg8::moe_gemm<pg8::EpiSwiGLU, true>(F.lds, F.w<bf16>(WS_XNB), F.w<int>(WS_LISTI), F.i_weg, F.i_weu, offs, cnts, So, E, F.wave);
; }
; __device__ __forceinline__ void ph_moe2(const Frame& F) {
;     LAS int* offs = (LAS int*)(F.lds + LDS_TAB); LAS int* cnts = offs + 128; LAS int* rt_exp = offs + 256;
;     expert_offsets(F, offs, cnts, rt_exp);
;     pg8::GroupedOrder So; So.init(rt_exp, (offs[64] >> 8) * 8, (int)gridDim.x, (int)blockIdx.x);
;     pg8::EpiMoeOut E{F.w<bf16>(WS_Y2), F.w<int>(WS_LISTI), F.w<float>(WS_LISTW), offs, cnts};
;     pg8::moe_gemm<pg8::EpiMoeOut, false>(F.lds, F.w<bf16>(WS_HID), F.w<int>(WS_LISTI), F.i_wed, F.i_wed, offs, cnts, So, E, F.wave);
.Lmoe_noremap:
	s_cmp_gt_u32 s86, 3
	s_cbranch_scc0 .Lmoe_prio_skip
	s_setprio 1

;     template <class Tp> __device__ __forceinline__ Tp* w(size_t off) const { return (Tp*)(ws + off); }
; __device__ __forceinline__ void ph_final(const Frame& F) {
;     const bf16* X2 = F.w<bf16>(WS_X2); const bf16* Y2 = F.w<bf16>(WS_Y2); const float* gf = F.i_final_g;
;     u32x2 xa[8], ya[8], yb[8], xn[8], yan[8], ybn[8];
;     float4 gw[8];
; #pragma unroll
;     for (int j = 0; j < 8; ++j) gw[j] = ((const float4*)gf)[F.lane + 64 * j];
;     int m = F.gw;
;     if (m < T) { const u32x2* xr = (const u32x2*)(X2 + (size_t)m * D); const u32x2* y0 = (const u32x2*)(Y2 + (size_t)(2 * m) * D); const u32x2* y1 = (const u32x2*)(Y2 + (size_t)(2 * m + 1) * D);
; #pragma unroll
;         for (int j = 0; j < 8; ++j) { xa[j] = __builtin_nontemporal_load(xr + F.lane + 64 * j); ya[j] = __builtin_nontemporal_load(y0 + F.lane + 64 * j); yb[j] = __builtin_nontemporal_load(y1 + F.lane + 64 * j); } }
;     for (; m < T; m += F.NGW) {
;         const int mn = m + F.NGW;
;         if (mn < T) { const u32x2* xr = (const u32x2*)(X2 + (size_t)mn * D); const u32x2* y0 = (const u32x2*)(Y2 + (size_t)(2 * mn) * D); const u32x2* y1 = (const u32x2*)(Y2 + (size_t)(2 * mn + 1) * D);
; #pragma unroll
;             for (int j = 0; j < 8; ++j) { xn[j] = __builtin_nontemporal_load(xr + F.lane + 64 * j); yan[j] = __builtin_nontemporal_load(y0 + F.lane + 64 * j); ybn[j] = __builtin_nontemporal_load(y1 + F.lane + 64 * j); } }
.LBB0_1396:
	s_setprio 0
	v_readlane_b32 s97, v248, 60
	s_cmp_lt_i32 s80, 10
	s_cselect_b64 s[0:1], -1, 0
	s_and_b64 s[0:1], s[0:1], s[2:3]
	s_andn2_b64 vcc, exec, s[0:1]
	s_cbranch_vccnz .LBB0_1402
	v_readlane_b32 s8, v248, 0
	v_readlane_b32 s9, v248, 1
	s_lshl_b32 s0, s97, 3
	s_add_i32 s4, s86, s0
	s_cmpk_gt_i32 s4, 0x3fff
	s_cbranch_scc1 .LBB0_1402
	v_readlane_b32 s0, v248, 0
	v_readlane_b32 s1, v248, 1
	s_load_dword s16, s[0:1], 0xd0
	s_load_dwordx2 s[10:11], s[8:9], 0xa8
	s_waitcnt vmcnt(0)
	v_mbcnt_lo_u32_b32 v0, -1, 0
	s_load_dwordx4 s[0:3], s[8:9], 0xb0
	v_mbcnt_hi_u32_b32 v40, -1, v0
	s_waitcnt lgkmcnt(0)
	s_lshl_b32 s6, s16, 3
	v_lshlrev_b32_e32 v34, 4, v40
	v_mov_b32_e32 v35, 0
	s_add_u32 s8, s2, 0xf000000
	s_addc_u32 s9, s3, 0
	s_ashr_i32 s5, s4, 31
	v_lshl_add_u64 v[16:17], s[10:11], 0, v[34:35]
	global_load_dwordx4 v[0:3], v34, s[10:11]
	global_load_dwordx4 v[4:7], v34, s[10:11] offset:1024
	global_load_dwordx4 v[8:11], v34, s[10:11] offset:2048
	global_load_dwordx4 v[12:15], v34, s[10:11] offset:3072
	s_lshl_b64 s[10:11], s[4:5], 12
	s_add_u32 s10, s2, s10
	s_addc_u32 s11, s3, s11
	s_lshl_b32 s12, s4, 1
	s_ashr_i32 s13, s12, 31
	s_lshl_b64 s[14:15], s[12:13], 12
	s_add_u32 s14, s8, s14
	v_add_co_u32_e32 v32, vcc, 0x1000, v16
	s_addc_u32 s15, s9, s15
	s_or_b32 s12, s12, 1
	v_addc_co_u32_e32 v33, vcc, 0, v17, vcc
	s_ashr_i32 s13, s12, 31
	v_lshlrev_b32_e32 v36, 3, v40
	v_mov_b32_e32 v37, v35
	global_load_dwordx4 v[16:19], v[32:33], off
	global_load_dwordx4 v[20:23], v[32:33], off offset:1024
	global_load_dwordx4 v[24:27], v[32:33], off offset:2048
	global_load_dwordx4 v[28:31], v[32:33], off offset:3072
	s_lshl_b64 s[12:13], s[12:13], 12
	v_lshl_add_u64 v[32:33], s[10:11], 0, v[36:37]
	s_mov_b64 s[10:11], 0x31000000
	s_mov_b32 s7, 0x31000000
	s_add_u32 s12, s8, s12
	v_lshl_add_u64 v[38:39], v[32:33], 0, s[10:11]
	v_add_co_u32_e32 v32, vcc, s7, v32
	s_addc_u32 s13, s9, s13
	s_nop 0
	v_addc_co_u32_e32 v33, vcc, 0, v33, vcc
	global_load_dwordx2 v[130:131], v36, s[14:15] nt
	global_load_dwordx2 v[124:125], v36, s[14:15] offset:512 nt
	global_load_dwordx2 v[118:119], v36, s[14:15] offset:1024 nt
	global_load_dwordx2 v[112:113], v36, s[14:15] offset:1536 nt
	global_load_dwordx2 v[128:129], v36, s[12:13] nt
	global_load_dwordx2 v[122:123], v36, s[12:13] offset:512 nt
	global_load_dwordx2 v[116:117], v36, s[12:13] offset:1024 nt
	global_load_dwordx2 v[106:107], v36, s[12:13] offset:1536 nt
	global_load_dwordx2 v[126:127], v[38:39], off offset:512 nt
	global_load_dwordx2 v[120:121], v[38:39], off offset:1024 nt
	global_load_dwordx2 v[114:115], v[38:39], off offset:1536 nt
	global_load_dwordx2 v[110:111], v[38:39], off offset:2048 nt
	global_load_dwordx2 v[132:133], v[32:33], off nt
	global_load_dwordx2 v[102:103], v[38:39], off offset:2560 nt
	global_load_dwordx2 v[96:97], v[38:39], off offset:3072 nt
	global_load_dwordx2 v[90:91], v[38:39], off offset:3584 nt
	global_load_dwordx2 v[108:109], v36, s[14:15] offset:2048 nt
	global_load_dwordx2 v[100:101], v36, s[14:15] offset:2560 nt
	global_load_dwordx2 v[94:95], v36, s[14:15] offset:3072 nt
	global_load_dwordx2 v[88:89], v36, s[14:15] offset:3584 nt
	global_load_dwordx2 v[104:105], v36, s[12:13] offset:2048 nt
	global_load_dwordx2 v[98:99], v36, s[12:13] offset:2560 nt
	global_load_dwordx2 v[92:93], v36, s[12:13] offset:3072 nt
	global_load_dwordx2 v[86:87], v36, s[12:13] offset:3584 nt
	v_and_b32_e32 v32, 64, v40
	v_add_u32_e32 v32, 64, v32
	v_xor_b32_e32 v33, 32, v40
	v_cmp_lt_i32_e32 vcc, v33, v32
	v_mov_b32_e32 v142, 0x358637bd
	s_nop 0
	v_cndmask_b32_e32 v33, v40, v33, vcc
	v_lshlrev_b32_e32 v136, 2, v33
	v_xor_b32_e32 v33, 16, v40
	v_cmp_lt_i32_e32 vcc, v33, v32
	s_nop 1
	v_cndmask_b32_e32 v33, v40, v33, vcc
	v_lshlrev_b32_e32 v137, 2, v33
	v_xor_b32_e32 v33, 8, v40
	v_cmp_lt_i32_e32 vcc, v33, v32
	s_nop 1
	v_cndmask_b32_e32 v33, v40, v33, vcc
	v_lshlrev_b32_e32 v138, 2, v33
	v_xor_b32_e32 v33, 4, v40
	v_cmp_lt_i32_e32 vcc, v33, v32
	s_nop 1
	v_cndmask_b32_e32 v33, v40, v33, vcc
	v_lshlrev_b32_e32 v139, 2, v33
	v_xor_b32_e32 v33, 2, v40
	v_cmp_lt_i32_e32 vcc, v33, v32
	s_nop 1
	v_cndmask_b32_e32 v33, v40, v33, vcc
	v_lshlrev_b32_e32 v140, 2, v33
	v_xor_b32_e32 v33, 1, v40
	v_cmp_lt_i32_e32 vcc, v33, v32
	s_nop 1
	v_cndmask_b32_e32 v32, v40, v33, vcc
	v_lshlrev_b32_e32 v141, 2, v32
	v_lshl_add_u64 v[32:33], s[8:9], 0, v[36:37]
	s_lshl_b64 s[8:9], s[4:5], 13
	s_add_u32 s0, s0, s8
	s_addc_u32 s1, s1, s9
	s_add_i32 s12, s4, s6
	v_lshl_add_u64 v[34:35], s[0:1], 0, v[34:35]
	s_mov_b64 s[0:1], 0x1000
	s_ashr_i32 s7, s6, 31
	s_ashr_i32 s13, s12, 31
	v_lshl_add_u64 v[34:35], v[34:35], 0, s[0:1]
	s_lshl_b64 s[0:1], s[6:7], 13
	s_lshl_b32 s8, s12, 1
	s_lshl_b32 s5, s16, 4
	s_lshl_b64 s[12:13], s[12:13], 12
	s_add_u32 s2, s2, s12
	s_addc_u32 s3, s3, s13
	v_lshl_add_u64 v[36:37], s[2:3], 0, v[36:37]
	v_lshl_add_u64 v[36:37], v[36:37], 0, s[10:11]
	s_lshl_b64 s[2:3], s[6:7], 12
	s_mov_b32 s7, 0x800000
	s_branch .LBB0_1400
